# attention loop stages the prologue's layer-0 items 0..0x2fff (6 per wave) plus all layer-1 items below 0xa800; the prologue stages no expert weights
# speedup vs baseline: 1.0062x; 1.0062x over previous
; #define LAS __attribute__((address_space(3)))
;     __device__ __forceinline__ const float* w_gate() const { return (const float*)ld(21); }
;     __device__ __forceinline__ const float* w_up() const { return (const float*)ld(22); }
;     __device__ __forceinline__ const float* w_down() const { return (const float*)ld(23); }
;     __device__ __forceinline__ unsigned char* ws() const { return (unsigned char*)ld(26); }
; __device__ __forceinline__ void convert_moe_items(const Ctx& a, int layer, LAS unsigned char* lds, int it0, int it1, int widx, int nw, int wave, int lane) {
;     LAS float* scr = (LAS float*)(lds + wave * 16384);
;     bf16_t* WGU = (bf16_t*)(a.ws() + WS_WGU + (size_t)layer * WGU_BYTES); bf16_t* WD = (bf16_t*)(a.ws() + WS_WD + (size_t)layer * WD_BYTES);
;     constexpr int I_G = (DM / 64) * (FE / 32), I_D = (FE / 64) * (DM / 32);
;     constexpr int PER_E = 2 * I_G + I_D;
;     const float *wg = a.w_gate(), *wu = a.w_up(), *wd = a.w_down();
;     auto decode = [&](int it) { CvtItem d; const int e = it / PER_E; int r = it % PER_E; const size_t eo = ((size_t)layer * NE + e) * (size_t)DM * FE;
;         if (r < I_G)          { d.src = wg + eo; d.dst = WGU; d.N = FE; d.K = DM; d.row_off = e * 2048; d.ilv = 1; }
;         else if (r < 2 * I_G) { r -= I_G; d.src = wu + eo; d.dst = WGU; d.N = FE; d.K = DM; d.row_off = e * 2048 + 128; d.ilv = 1; }
;         else                  { r -= 2 * I_G; d.src = wd + eo; d.dst = WD; d.N = DM; d.K = FE; d.row_off = e * 2048; d.ilv = 0; }
;         const int nblk = d.N / 32; d.k0 = 64 * (r / nblk); d.n0 = 32 * (r % nblk); return d; };
;     int it = it0 + widx;
;     if (it >= it1) return;
;     f32x4 va[8], vb[8]; CvtItem da = decode(it), db = da; bool hb = (it + nw < it1);
;     cvt_load(da, va, lane);
;     if (hb) { db = decode(it + nw); cvt_load(db, vb, lane); }
; __device__ __forceinline__ void p0_prologue(const Ctx& a, LAS unsigned char* lds, int G) {
;     ...
;         convert_moe_items(a, 0, lds, 0, L0_A, gw, NGW, wave, lane);
.LBB0_127:
	s_add_i32 s0, 0, 0x23f10
	s_waitcnt vmcnt(7)
	v_mov_b32_e32 v2, s0
	s_waitcnt vmcnt(6)
	ds_read_b64 v[6:7], v2
	s_add_i32 s0, 0, 0x23ee8
	v_mov_b32_e32 v2, s0
	s_add_i32 s0, 0, 0x23ef8
	ds_read2_b64 v[2:5], v2 offset1:1
	s_waitcnt lgkmcnt(1)
	v_readfirstlane_b32 s3, v6
	v_mov_b32_e32 v6, s0
	v_readfirstlane_b32 s2, v7
	ds_read_b64 v[6:7], v6
	s_waitcnt lgkmcnt(1)
	v_readfirstlane_b32 s29, v3
	v_readfirstlane_b32 s30, v2
	v_readfirstlane_b32 s31, v5
	v_readfirstlane_b32 s33, v4
	s_waitcnt lgkmcnt(0)
	v_readfirstlane_b32 s34, v7
	s_cmpk_gt_i32 s28, 0x2fff
	v_readfirstlane_b32 s35, v6
	s_branch .LBB0_168
	s_add_u32 s0, s3, 0x2530000
	s_addc_u32 s1, s2, 0
	s_add_u32 s4, s3, 0x12530000
	s_addc_u32 s5, s2, 0
	s_mul_hi_i32 s2, s28, 0x2aaaaaab
	s_lshr_b32 s3, s2, 31
	s_ashr_i32 s2, s2, 9
	s_add_i32 s2, s2, s3
	s_mul_i32 s3, s2, 0xc00
	s_sub_i32 s13, s28, s3
	s_ashr_i32 s3, s2, 31
	s_lshl_b64 s[8:9], s[2:3], 21
	s_lshl_b32 s17, s2, 11
	s_cmpk_gt_i32 s13, 0x3ff
	s_cbranch_scc0 .LBB0_132
	s_cmpk_gt_u32 s13, 0x7ff
	s_cbranch_scc0 .LBB0_139
	s_add_i32 s16, s13, 0xfffff800
	s_lshl_b64 s[2:3], s[8:9], 2
	s_add_u32 s2, s35, s2
	s_addc_u32 s3, s34, s3
	s_mov_b32 s27, 1
	s_cbranch_execz .LBB0_140
	s_movk_i32 s12, 0x800
	s_movk_i32 s36, 0x400
	s_mov_b32 s27, 0
	s_mov_b32 s37, s17
	s_mov_b64 s[6:7], s[4:5]
	s_cbranch_execz .LBB0_133
	s_branch .LBB0_134

; #define LAS __attribute__((address_space(3)))
; #define WAIT_BAR(N) asm volatile("s_waitcnt vmcnt(" #N ") lgkmcnt(0)\n\ts_barrier" ::: "memory")
;     __device__ __forceinline__ const float* x() const { return (const float*)ld(0); }
; template <int THRL> ...
;   const int tid = threadIdx.x, lane = tid & 63, r32 = lane & 31, hi = lane >> 5; const int wid = __builtin_amdgcn_readfirstlane(tid >> 6);
;   const int comp = wid >> 2, wq = wid & 3;
;   if (wid >= 4) __builtin_amdgcn_s_setprio(1);
;   const bf16_t* Qw = Q + (size_t)(CTXL + qb * 128 + wq * QBLK) * DMK + head * 128 + comp * 64;
;   const bf16_t* Kh = K + head * 128; const bf16_t* Vh = V + head * 128;
;   const unsigned lds0 = (unsigned)(uintptr_t)shm;
;   LAS float* wsf = (LAS float*)(shm + LDS_WS) + wid * 64;
;   const unsigned kvoff = (unsigned)(lane * DMK + wid * 8) * 2u;
;   const unsigned vvoff = (unsigned)((16 * (wid & 3) + (lane >> 2)) * DMK + (wid >> 2) * 32 + (lane & 3) * 8) * 2u;
;   const unsigned kdst = lds0 + LDS_K + wid * 1024, vdst = lds0 + LDS_V + wid * 1024;
;     ...
;   const int vb0 = (int)(lds0 + LDS_V) + ((lane >> 4) & 1) * 32 + (lane & 3) * 8 + (4 * hi + ((lane & 15) >> 2)) * 64;
;   bf16x8 kf[8];
;   const lds_cptr shm3 = (lds_cptr)shm; const lds_cptr kp0 = shm3 + LDS_K + comp * 8192 + hi * 1024 + r32 * 16;
;   const lds_cptr vp0 = shm3 + LDS_V + ((lane >> 4) & 1) * 32 + (lane & 3) * 8 + (4 * hi + ((lane & 15) >> 2)) * 64;
;   DMA_K(0, 0); DMA_V(0, 0); DMA_K(1, SLOTB);
;   bf16x8 qr[4];
; #pragma unroll
;   for (int d0 = 0; d0 < 4; ++d0) qr[d0] = *reinterpret_cast<const bf16x8*>(&Qw[(long)r32 * DMK + d0 * 16 + hi * 8]);
;   float mhat = 0.f, l_reg = 0.f; f32x16 o[4]; o[0] = f32x16{}; o[1] = f32x16{}; o[2] = f32x16{}; o[3] = f32x16{}; f32x16 negm = f32x16{}; asm volatile("" : "+v"(negm));
;   bool resc = false;
;     ...
;   f32x16 pA0, pA1, pB0, pB1;
;   int sl_prev = 0, sl_cur = 0, sl_next = SLOTB;
;     ...
;   DMA_K(2, 2 * SLOTB);
;   WAIT_BAR(6);
;   qkt(pA0, pA1, kp0, qr, negm); asm volatile("s_nop 15\n\ts_nop 7" : "+v"(pA0), "+v"(pA1));
;   const lds_cptr qp = shm3 + LDS_Q + wid * 4096 + lane * 16;
; #pragma unroll
;   for (int d0 = 0; d0 < 4; ++d0) *(LAS bf16x8*)(shm + LDS_Q + wid * 4096 + lane * 16 + d0 * 1024) = qr[d0];
;   START(pA0, pA1);
.LBB0_527:
	s_lshl_b32 s0, s28, 1
	s_and_b32 s0, s0, 0x700
	s_add_u32 s33, s26, s0
	s_addc_u32 s53, s27, 0
	s_bfe_u32 s41, s39, 0x20006
	s_lshl_b32 s0, s36, 4
	s_and_b32 s37, s0, 0xffffff80
	s_lshl_b32 s0, s41, 5
	s_or_b32 s0, s37, s0
	s_addk_i32 s0, 0x100
	s_ashr_i32 s1, s0, 31
	s_lshr_b32 s40, s39, 6
	s_lshr_b32 s42, s39, 8
	s_lshl_b64 s[0:1], s[0:1], 11
	s_add_u32 s0, s5, s0
	s_addc_u32 s1, s17, s1
	s_lshl_b32 s2, s36, 7
	s_and_b32 s14, s2, 0x380
	s_lshl_b32 s8, s14, 1
	s_add_u32 s0, s0, s8
	s_addc_u32 s1, s1, 0
	s_lshl_b32 s43, s42, 6
	s_lshl_b32 s2, s42, 7
	s_add_u32 s2, s0, s2
	s_addc_u32 s3, s1, 0
	s_add_u32 s20, s22, s8
	s_addc_u32 s21, s23, 0
	s_add_u32 s8, s24, s8
	s_addc_u32 s9, s25, 0
	s_lshl_b32 s0, s41, 15
	s_add_i32 s0, s0, s43
	v_add_u32_e32 v235, s0, v219
	s_lshl_b32 s0, s40, 10
	s_add_i32 s49, s0, 0
	s_and_b32 s1, s39, 0x3fffffc0
	s_lshl_b32 s38, s40, 4
	s_add_i32 s46, s49, 0xc000
	s_add_u32 s44, s20, 0x80
	v_add_u32_e32 v237, s38, v218
	s_mov_b32 s0, m0
	s_mov_b32 m0, s49
	s_nop 0
	global_load_lds_dwordx4 v237, s[20:21] offset:0
	s_mov_b32 m0, s0
	s_addc_u32 s45, s21, 0
	s_add_i32 s54, s49, 0x2000
	s_mov_b32 s0, m0
	s_mov_b32 m0, s54
	s_nop 0
	global_load_lds_dwordx4 v237, s[44:45] offset:0
	s_mov_b32 m0, s0
	s_add_u32 s50, s8, 0x80
	s_mov_b32 s0, m0
	s_mov_b32 m0, s46
	s_nop 0
	global_load_lds_dwordx4 v235, s[8:9] offset:0
	s_mov_b32 m0, s0
	s_addc_u32 s51, s9, 0
	s_add_i32 s45, s49, 0xe000
	s_mov_b32 s0, m0
	s_mov_b32 m0, s45
	s_nop 0
	global_load_lds_dwordx4 v235, s[50:51] offset:0
	s_mov_b32 m0, s0
	s_add_u32 s50, s20, 0x20000
	s_addc_u32 s51, s21, 0
	s_add_i32 s52, s49, 0x4000
	s_mov_b32 s0, m0
	s_mov_b32 m0, s52
	s_nop 0
	global_load_lds_dwordx4 v237, s[50:51] offset:0
	s_mov_b32 m0, s0
	s_add_u32 s56, s20, 0x20080
	s_addc_u32 s57, s21, 0
	s_add_i32 s51, s49, 0x6000
	s_mov_b32 s0, m0
	s_mov_b32 m0, s51
	s_nop 0
	global_load_lds_dwordx4 v237, s[56:57] offset:0
	s_mov_b32 m0, s0
	global_load_dwordx4 v[66:69], v229, s[2:3]
	global_load_dwordx4 v[70:73], v229, s[2:3] offset:32
	global_load_dwordx4 v[74:77], v229, s[2:3] offset:64
	global_load_dwordx4 v[78:81], v229, s[2:3] offset:96
	v_mov_b64_e32 v[48:49], v[32:33]
	s_add_u32 s2, s20, 0x40000
	v_mov_b64_e32 v[46:47], v[30:31]
	v_mov_b64_e32 v[44:45], v[28:29]
	v_mov_b64_e32 v[42:43], v[26:27]
	v_mov_b64_e32 v[40:41], v[24:25]
	v_mov_b64_e32 v[38:39], v[22:23]
	v_mov_b64_e32 v[36:37], v[20:21]
	v_mov_b64_e32 v[34:35], v[18:19]
	s_addc_u32 s3, s21, 0
	s_add_i32 s48, s49, 0x8000
	s_mov_b32 s0, m0
	s_mov_b32 m0, s48
	s_nop 0
	global_load_lds_dwordx4 v237, s[2:3] offset:0
	s_mov_b32 m0, s0
	s_add_u32 s2, s20, 0x40080
	s_addc_u32 s3, s21, 0
	s_add_i32 s47, s49, 0xa000
	s_mov_b32 s0, m0
	s_mov_b32 m0, s47
	s_nop 0
	global_load_lds_dwordx4 v237, s[2:3] offset:0
	s_mov_b32 m0, s0
	v_lshl_add_u32 v236, s42, 13, v221
	s_waitcnt vmcnt(6) lgkmcnt(0)
	s_barrier
	ds_read_b128 v[4:7], v236
	s_lshl_b32 s2, s40, 12
	v_add_u32_e32 v233, s2, v222
	s_lshl_b32 s1, s1, 2
	s_add_i32 s50, s1, 0
	s_add_i32 s50, s50, 0x18000
	s_add_u32 s2, s20, 0x60000
	s_addc_u32 s3, s21, 0
	v_mov_b32_e32 v3, v2
	v_mov_b32_e32 v12, v2
	v_mov_b32_e32 v13, v2
	s_movk_i32 s57, 0x4000
	s_mov_b32 s0, 0
	s_mov_b32 s55, 0x8000
	v_lshl_add_u32 v232, v217, 2, s50
	v_mov_b32_e32 v238, 0
	s_mov_b32 s56, -1
	s_waitcnt vmcnt(3) lgkmcnt(0)
	v_mfma_f32_32x32x16_bf16 v[50:65], v[4:7], v[66:69], v[34:49]
	ds_read_b128 v[4:7], v236 offset:512
	s_waitcnt lgkmcnt(0)
	v_mfma_f32_32x32x16_bf16 v[34:49], v[4:7], v[66:69], v[34:49]
	ds_read_b128 v[4:7], v236 offset:2048
	s_waitcnt vmcnt(2) lgkmcnt(0)
	v_mfma_f32_32x32x16_bf16 v[50:65], v[4:7], v[70:73], v[50:65]
	ds_read_b128 v[4:7], v236 offset:2560
	s_waitcnt lgkmcnt(0)
	v_mfma_f32_32x32x16_bf16 v[34:49], v[4:7], v[70:73], v[34:49]
	ds_read_b128 v[4:7], v236 offset:4096
	ds_read_b128 v[8:11], v236 offset:4608
	ds_read_b128 v[82:85], v236 offset:6656
	ds_read_b128 v[14:17], v236 offset:6144
	s_waitcnt vmcnt(1) lgkmcnt(3)
	v_mfma_f32_32x32x16_bf16 v[50:65], v[4:7], v[74:77], v[50:65]
	v_mov_b32_e32 v4, v2
	v_mov_b32_e32 v5, v2
	v_mov_b32_e32 v6, v2
	v_mov_b32_e32 v7, v2
	s_waitcnt lgkmcnt(2)
	v_mfma_f32_32x32x16_bf16 v[34:49], v[8:11], v[74:77], v[34:49]
	v_mov_b32_e32 v8, v2
	v_mov_b32_e32 v9, v2
	v_mov_b32_e32 v10, v2
	v_mov_b32_e32 v11, v2
	s_waitcnt vmcnt(0) lgkmcnt(0)
	v_mfma_f32_32x32x16_bf16 v[50:65], v[14:17], v[78:81], v[50:65]
	v_mov_b32_e32 v16, v2
	v_mov_b32_e32 v17, v2
	v_mov_b32_e32 v14, v2
	v_mov_b32_e32 v15, v2
	v_mfma_f32_32x32x16_bf16 v[34:49], v[82:85], v[78:81], v[34:49]
	s_nop 15
	s_nop 7
	ds_write_b128 v233, v[66:69]
	ds_write_b128 v233, v[70:73] offset:1024
	ds_write_b128 v233, v[74:77] offset:2048
	ds_write_b128 v233, v[78:81] offset:3072
	v_max3_f32 v66, v50, v51, v34
	v_max3_f32 v67, v52, v53, v35
	v_mov_b64_e32 v[96:97], v[16:17]
	v_max3_f32 v66, v66, v36, v37
	v_max3_f32 v67, v67, v56, v57
	v_mov_b64_e32 v[94:95], v[14:15]
	v_max3_f32 v66, v66, v54, v55
	v_max3_f32 v67, v67, v40, v41
	v_mov_b64_e32 v[92:93], v[12:13]
	v_max3_f32 v66, v66, v38, v39
	v_max3_f32 v67, v67, v60, v61
	v_mov_b64_e32 v[90:91], v[10:11]
	v_max3_f32 v66, v66, v58, v59
	v_max3_f32 v67, v67, v44, v45
	v_mov_b64_e32 v[88:89], v[8:9]
	v_max3_f32 v66, v66, v42, v43
	v_max3_f32 v67, v67, v64, v65
	v_mov_b64_e32 v[86:87], v[6:7]
	v_max3_f32 v66, v66, v62, v63
	v_max3_f32 v67, v67, v48, v49
	v_mov_b64_e32 v[84:85], v[4:5]
	v_max3_f32 v66, v66, v46, v47
	v_mov_b64_e32 v[82:83], v[2:3]
	v_max_f32_e32 v66, v66, v67
	s_nop 0
	v_mov_b32_e32 v67, v66
	s_nop 1
	v_permlane32_swap_b32_e32 v66, v67
	v_max_f32_e32 v66, v66, v67
	s_nop 0
	v_add_f32_e32 v234, v2, v66
	v_sub_f32_e32 v50, v50, v66
	v_sub_f32_e32 v34, v34, v66
	v_sub_f32_e32 v51, v51, v66
	v_sub_f32_e32 v35, v35, v66
	v_sub_f32_e32 v52, v52, v66
	s_nop 0
	v_xor_b32_e32 v98, 0x80000000, v234
	v_mov_b32_e32 v99, v98
	v_mov_b32_e32 v100, v98
	v_mov_b32_e32 v101, v98
	v_mov_b32_e32 v102, v98
	v_mov_b32_e32 v103, v98
	v_mov_b32_e32 v104, v98
	v_mov_b32_e32 v105, v98
	v_mov_b32_e32 v106, v98
	v_mov_b32_e32 v107, v98
	v_mov_b32_e32 v108, v98
	v_mov_b32_e32 v109, v98
	v_mov_b32_e32 v110, v98
	v_mov_b32_e32 v111, v98
	v_mov_b32_e32 v112, v98
	v_mov_b32_e32 v113, v98
	s_waitcnt vmcnt(0) lgkmcnt(0)
	s_barrier
; #define LAS __attribute__((address_space(3)))
; #define WAIT_BAR(N) asm volatile("s_waitcnt vmcnt(" #N ") lgkmcnt(0)\n\ts_barrier" ::: "memory")
; #define DMA_K(t, slot) do { const bf16_t* sb_ = Kh + (long)(t) * KVBLK * DMK; glds16<0>(sb_, kvoff, (unsigned)__builtin_amdgcn_readfirstlane(kdst + (slot))); glds16<0>(sb_ + 64, kvoff, (unsigned)__builtin_amdgcn_readfirstlane(kdst + 8192 + (slot))); } while (0)
; #define DMA_V(t, slot) do { const bf16_t* sb_ = Vh + (long)(t) * KVBLK * DMK; glds16<0>(sb_, vvoff, (unsigned)__builtin_amdgcn_readfirstlane(vdst + (slot))); glds16<0>(sb_ + 64, vvoff, (unsigned)__builtin_amdgcn_readfirstlane(vdst + 8192 + (slot))); } while (0)
; #define ROT() do { sl_prev = sl_cur; sl_cur = sl_next; sl_next = (sl_next == (NSLOT - 1) * SLOTB) ? 0 : sl_next + SLOTB; } while (0)
;     __device__ __forceinline__ const float* w_gate() const { return (const float*)ld(21); }
; template <int THRL> ...
;     ...
;   START(pA0, pA1);
; #pragma unroll
;   for (int r = 0; r < 16; ++r) pA1[r] = __builtin_amdgcn_exp2f(pA1[r]);
;   WAIT_BAR(0);
;   DMA_K(3, 0); DMA_V(1, SLOTB);
;   ROT();
;   kload8(kf, kp0 + sl_cur);
;   WAIT_BAR(4);
; __device__ __forceinline__ void convert_moe_items(const Ctx& a, int layer, LAS unsigned char* lds, int it0, int it1, int widx, int nw, int wave, int lane) {
;     LAS float* scr = (LAS float*)(lds + wave * 16384);
;     bf16_t* WGU = (bf16_t*)(a.ws() + WS_WGU + (size_t)layer * WGU_BYTES); bf16_t* WD = (bf16_t*)(a.ws() + WS_WD + (size_t)layer * WD_BYTES);
;     constexpr int I_G = (DM / 64) * (FE / 32), I_D = (FE / 64) * (DM / 32);
;     constexpr int PER_E = 2 * I_G + I_D;
;     const float *wg = a.w_gate(), *wu = a.w_up(), *wd = a.w_down();
;     auto decode = [&](int it) { CvtItem d; const int e = it / PER_E; int r = it % PER_E; const size_t eo = ((size_t)layer * NE + e) * (size_t)DM * FE;
;         if (r < I_G)          { d.src = wg + eo; d.dst = WGU; d.N = FE; d.K = DM; d.row_off = e * 2048; d.ilv = 1; }
;         else if (r < 2 * I_G) { r -= I_G; d.src = wu + eo; d.dst = WGU; d.N = FE; d.K = DM; d.row_off = e * 2048 + 128; d.ilv = 1; }
;         else                  { r -= 2 * I_G; d.src = wd + eo; d.dst = WD; d.N = DM; d.K = FE; d.row_off = e * 2048; d.ilv = 0; }
;         const int nblk = d.N / 32; d.k0 = 64 * (r / nblk); d.n0 = 32 * (r % nblk); return d; };
;     int it = it0 + widx;
	s_mov_b32 s1, m0
	s_mov_b32 m0, s49
	s_nop 0
	global_load_lds_dwordx4 v237, s[2:3] offset:0
	s_mov_b32 m0, s1
	s_add_u32 s2, s20, 0x60080
	s_addc_u32 s3, s21, 0
	s_mov_b32 s1, m0
	s_mov_b32 m0, s54
	s_nop 0
	global_load_lds_dwordx4 v237, s[2:3] offset:0
	s_mov_b32 m0, s1
	s_add_u32 s2, s8, 0x20000
	s_addc_u32 s3, s9, 0
	s_add_i32 s44, s49, 0x10000
	s_mov_b32 s1, m0
	s_mov_b32 m0, s44
	s_nop 0
	global_load_lds_dwordx4 v235, s[2:3] offset:0
	s_mov_b32 m0, s1
	s_add_u32 s2, s8, 0x20080
	s_addc_u32 s3, s9, 0
	s_add_i32 s43, s49, 0x12000
	s_mov_b32 s1, m0
	s_mov_b32 m0, s43
	s_nop 0
	global_load_lds_dwordx4 v235, s[2:3] offset:0
	s_mov_b32 m0, s1
	ds_read_b128 v[146:149], v236 offset:16384
	ds_read_b128 v[202:205], v236 offset:16896
	ds_read_b128 v[206:209], v236 offset:18432
	ds_read_b128 v[190:193], v236 offset:18944
	ds_read_b128 v[198:201], v236 offset:20480
	ds_read_b128 v[186:189], v236 offset:20992
	ds_read_b128 v[182:185], v236 offset:22528
	ds_read_b128 v[178:181], v236 offset:23040
	v_sub_f32_e32 v36, v36, v66
	v_sub_f32_e32 v53, v53, v66
	v_sub_f32_e32 v37, v37, v66
	v_sub_f32_e32 v54, v54, v66
	v_sub_f32_e32 v38, v38, v66
	v_sub_f32_e32 v55, v55, v66
	v_sub_f32_e32 v39, v39, v66
	v_sub_f32_e32 v56, v56, v66
	v_sub_f32_e32 v40, v40, v66
	v_sub_f32_e32 v57, v57, v66
	v_sub_f32_e32 v41, v41, v66
	v_sub_f32_e32 v58, v58, v66
	v_sub_f32_e32 v42, v42, v66
	v_sub_f32_e32 v59, v59, v66
	v_sub_f32_e32 v43, v43, v66
	v_sub_f32_e32 v60, v60, v66
	v_sub_f32_e32 v44, v44, v66
	v_sub_f32_e32 v61, v61, v66
	v_sub_f32_e32 v45, v45, v66
	v_sub_f32_e32 v62, v62, v66
	v_sub_f32_e32 v46, v46, v66
	v_sub_f32_e32 v63, v63, v66
	v_sub_f32_e32 v47, v47, v66
	v_sub_f32_e32 v64, v64, v66
	v_sub_f32_e32 v48, v48, v66
	v_sub_f32_e32 v65, v65, v66
	v_sub_f32_e32 v49, v49, v66
	v_exp_f32_e32 v130, v50
	v_exp_f32_e32 v131, v51
	v_exp_f32_e32 v132, v52
	v_exp_f32_e32 v133, v53
	v_exp_f32_e32 v134, v54
	v_exp_f32_e32 v135, v55
	v_exp_f32_e32 v136, v56
	v_exp_f32_e32 v137, v57
	v_exp_f32_e32 v138, v58
	v_exp_f32_e32 v139, v59
	v_exp_f32_e32 v140, v60
	v_exp_f32_e32 v141, v61
	v_exp_f32_e32 v142, v62
	v_exp_f32_e32 v143, v63
	v_exp_f32_e32 v144, v64
	v_exp_f32_e32 v145, v65
	v_exp_f32_e32 v114, v34
	v_exp_f32_e32 v115, v35
	v_exp_f32_e32 v116, v36
	v_exp_f32_e32 v117, v37
	v_exp_f32_e32 v118, v38
	v_exp_f32_e32 v119, v39
	v_exp_f32_e32 v120, v40
	v_exp_f32_e32 v121, v41
	v_exp_f32_e32 v122, v42
	v_exp_f32_e32 v123, v43
	v_exp_f32_e32 v124, v44
	v_exp_f32_e32 v125, v45
	v_exp_f32_e32 v126, v46
	v_exp_f32_e32 v127, v47
	v_exp_f32_e32 v128, v48
	v_exp_f32_e32 v129, v49
	s_waitcnt vmcnt(4) lgkmcnt(0)
	s_barrier
	v_mov_b64_e32 v[80:81], v[16:17]
	v_mov_b64_e32 v[48:49], v[16:17]
	v_mov_b64_e32 v[64:65], v[16:17]
	v_mov_b64_e32 v[78:79], v[14:15]
	v_mov_b64_e32 v[76:77], v[12:13]
	v_mov_b64_e32 v[74:75], v[10:11]
	v_mov_b64_e32 v[72:73], v[8:9]
	v_mov_b64_e32 v[70:71], v[6:7]
	v_mov_b64_e32 v[68:69], v[4:5]
	v_mov_b64_e32 v[66:67], v[2:3]
	v_mov_b64_e32 v[46:47], v[14:15]
	v_mov_b64_e32 v[44:45], v[12:13]
	v_mov_b64_e32 v[42:43], v[10:11]
	v_mov_b64_e32 v[40:41], v[8:9]
	v_mov_b64_e32 v[38:39], v[6:7]
	v_mov_b64_e32 v[36:37], v[4:5]
	v_mov_b64_e32 v[34:35], v[2:3]
	v_mov_b64_e32 v[62:63], v[14:15]
	v_mov_b64_e32 v[60:61], v[12:13]
	v_mov_b64_e32 v[58:59], v[10:11]
	v_mov_b64_e32 v[56:57], v[8:9]
	v_mov_b64_e32 v[54:55], v[6:7]
	v_mov_b64_e32 v[52:53], v[4:5]
	v_mov_b64_e32 v[50:51], v[2:3]
	v_mov_b32_e32 v244, 0x23ee8
	ds_read2_b64 v[250:253], v244 offset1:1
	ds_read_b64 v[254:255], v244 offset:16
	s_waitcnt lgkmcnt(0)
	v_readfirstlane_b32 s68, v250
	v_readfirstlane_b32 s69, v251
	v_readfirstlane_b32 s70, v252
	v_readfirstlane_b32 s71, v253
	v_readfirstlane_b32 s72, v254
	v_readfirstlane_b32 s73, v255
	ds_read_b64 v[250:251], v244 offset:40
	s_waitcnt lgkmcnt(0)
	v_readfirstlane_b32 s74, v250
	v_readfirstlane_b32 s75, v251
	s_add_u32 s76, s74, 0x16530000
	s_addc_u32 s77, s75, 0
	s_add_u32 s74, s74, 0xa530000
	s_addc_u32 s75, s75, 0
	v_lshrrev_b32_e32 v25, 3, v214
	v_and_b32_e32 v28, 7, v214
	v_lshlrev_b32_e32 v33, 4, v28
	v_lshl_add_u32 v24, v25, 12, v33
	v_lshl_add_u32 v246, v25, 13, v33
	v_lshlrev_b32_e32 v29, 8, v28
	v_lshl_add_u32 v29, v25, 1, v29
	s_lshl_b32 s2, s40, 11
	s_cmp_lt_u32 s40, 6
	s_mov_b32 s3, 0x21000
	s_cselect_b32 s3, 0x20800, s3
	s_add_i32 s2, s2, s3
	v_add_u32_e32 v29, s2, v29
	v_add_u32_e32 v29, 32, v29
	v_lshl_add_u32 v32, v214, 3, s2
	s_mul_i32 s66, s96, 8
	s_add_i32 s66, s66, s40
	s_cmpk_lt_u32 s36, 0x100
	s_movk_i32 s67, 104
	s_cselect_b32 s67, 112, s67
	s_cselect_b32 s2, 0, 0x7000
	s_add_i32 s66, s66, s2
	s_add_i32 s90, s67, 6
	s_cmp_eq_u32 s67, 0
	s_cselect_b32 s90, -1, s90
	global_load_dword v249, v24, s[68:69]
	global_load_dword v249, v24, s[68:69]

; __device__ __forceinline__ void convert_moe_items(const Ctx& a, int layer, LAS unsigned char* lds, int it0, int it1, int widx, int nw, int wave, int lane) {
;     ...
;     auto decode = [&](int it) { CvtItem d; const int e = it / PER_E; int r = it % PER_E; const size_t eo = ((size_t)layer * NE + e) * (size_t)DM * FE;
;         if (r < I_G)          { d.src = wg + eo; d.dst = WGU; d.N = FE; d.K = DM; d.row_off = e * 2048; d.ilv = 1; }
;         else if (r < 2 * I_G) { r -= I_G; d.src = wu + eo; d.dst = WGU; d.N = FE; d.K = DM; d.row_off = e * 2048 + 128; d.ilv = 1; }
;         else                  { r -= 2 * I_G; d.src = wd + eo; d.dst = WD; d.N = DM; d.K = FE; d.row_off = e * 2048; d.ilv = 0; }
;         const int nblk = d.N / 32; d.k0 = 64 * (r / nblk); d.n0 = 32 * (r % nblk); return d; };
.Lcs_dec_h0:
	s_cmp_lt_u32 s66, 0xa800
	s_cbranch_scc1 .Lcs_id_h0
	s_bitcmp1_b32 s66, 16
	s_cbranch_scc1 .Lcs_id_h0
	s_add_i32 s66, s66, 0x5800
